# baseline (speedup 1.0000x reference)
.LBB0_120:
	s_cmpk_gt_u32 s33, 0x7f
	s_waitcnt lgkmcnt(0)
	s_cbranch_scc1 .Lmlp_others
	v_mbcnt_lo_u32_b32 v92, -1, 0
	v_mbcnt_hi_u32_b32 v92, -1, v92
	v_mov_b32_e32 v1, 0x15300
	v_ashrrev_i32_e32 v0, 5, v92
	s_waitcnt vmcnt(0)
	v_and_or_b32 v37, v92, 31, s31
	v_lshlrev_b32_e32 v38, 4, v0
	v_lshl_add_u32 v1, v37, 2, v1
	v_add_u32_e32 v93, 0x14c00, v38
	ds_read_b32 v36, v1
	ds_read_b128 v[0:3], v93
	ds_read_b128 v[4:7], v93 offset:32
	ds_read_b128 v[8:11], v93 offset:64
	v_add_u32_e32 v39, v93, v38
	ds_read_b128 v[24:27], v39 offset:1280
	ds_read_b128 v[28:31], v39 offset:1024
	ds_read_b128 v[12:15], v93 offset:96
	ds_read_b128 v[16:19], v93 offset:128
	ds_read_b128 v[20:23], v39 offset:1040
	ds_read_b128 v[32:35], v39 offset:1232
	ds_read_b128 v[80:83], v93 offset:992
	s_waitcnt lgkmcnt(5)
	v_fma_f32 v24, v36, v28, v24
	v_max_f32_e32 v44, 0, v24
	v_fma_f32 v24, v36, v29, v25
	ds_read_b128 v[40:43], v39 offset:1296
	v_max_f32_e32 v45, 0, v24
	v_fma_f32 v24, v36, v30, v26
	v_fmac_f32_e32 v27, v36, v31
	v_max_f32_e32 v46, 0, v24
	v_max_f32_e32 v47, 0, v27
	ds_read_b128 v[24:27], v39 offset:1088
	ds_read_b128 v[28:31], v39 offset:1344
	s_waitcnt lgkmcnt(2)
	v_fma_f32 v20, v36, v20, v40
	v_fma_f32 v21, v36, v21, v41
	v_max_f32_e32 v20, 0, v20
	v_max_f32_e32 v21, 0, v21
	v_fma_f32 v22, v36, v22, v42
	v_cvt_pk_f16_f32 v42, v20, v21
	s_waitcnt lgkmcnt(0)
	v_fma_f32 v20, v36, v24, v28
	v_fmac_f32_e32 v43, v36, v23
	v_max_f32_e32 v48, 0, v20
	v_fma_f32 v20, v36, v25, v29
	v_max_f32_e32 v22, 0, v22
	v_max_f32_e32 v23, 0, v43
	v_max_f32_e32 v49, 0, v20
	v_fma_f32 v20, v36, v26, v30
	v_cvt_pk_f16_f32 v43, v22, v23
	v_cvt_pk_f16_f32 v41, v46, v47
	v_cvt_pk_f16_f32 v40, v44, v45
	v_max_f32_e32 v50, 0, v20
	ds_read_b128 v[20:23], v39 offset:1104
	ds_read_b128 v[44:47], v39 offset:1360
	v_fmac_f32_e32 v31, v36, v27
	v_max_f32_e32 v51, 0, v31
	ds_read_b128 v[24:27], v39 offset:1152
	ds_read_b128 v[28:31], v39 offset:1408
	v_lshlrev_b32_e32 v94, 4, v92
	s_waitcnt lgkmcnt(2)
	v_fma_f32 v20, v36, v20, v44
	v_fma_f32 v21, v36, v21, v45
	v_max_f32_e32 v20, 0, v20
	v_max_f32_e32 v21, 0, v21
	v_fma_f32 v22, v36, v22, v46
	v_cvt_pk_f16_f32 v46, v20, v21
	s_waitcnt lgkmcnt(0)
	v_fma_f32 v20, v36, v24, v28
	v_fmac_f32_e32 v47, v36, v23
	v_max_f32_e32 v52, 0, v20
	v_fma_f32 v20, v36, v25, v29
	v_max_f32_e32 v22, 0, v22
	v_max_f32_e32 v23, 0, v47
	v_max_f32_e32 v53, 0, v20
	v_fma_f32 v20, v36, v26, v30
	v_cvt_pk_f16_f32 v47, v22, v23
	v_cvt_pk_f16_f32 v45, v50, v51
	v_cvt_pk_f16_f32 v44, v48, v49
	v_max_f32_e32 v54, 0, v20
	ds_read_b128 v[20:23], v39 offset:1168
	ds_read_b128 v[48:51], v39 offset:1424
	v_fmac_f32_e32 v31, v36, v27
	v_max_f32_e32 v55, 0, v31
	ds_read_b128 v[24:27], v39 offset:1216
	ds_read_b128 v[28:31], v39 offset:1472
	v_cvt_pk_f16_f32 v84, v52, v53
	s_waitcnt lgkmcnt(2)
	v_fma_f32 v20, v36, v20, v48
	v_fma_f32 v21, v36, v21, v49
	v_fma_f32 v22, v36, v22, v50
	v_fmac_f32_e32 v51, v36, v23
	v_max_f32_e32 v20, 0, v20
	v_max_f32_e32 v21, 0, v21
	v_max_f32_e32 v22, 0, v22
	v_max_f32_e32 v23, 0, v51
	v_cvt_pk_f16_f32 v87, v22, v23
	v_cvt_pk_f16_f32 v86, v20, v21
	ds_read_b128 v[20:23], v94
	ds_read_b128 v[48:51], v94 offset:1024
	s_waitcnt lgkmcnt(1)
	v_mfma_f32_32x32x16_f16 v[0:15], v[20:23], v[40:43], v[0:15]
	v_fma_f32 v24, v36, v24, v28
	v_max_f32_e32 v52, 0, v24
	v_fma_f32 v24, v36, v25, v29
	v_max_f32_e32 v53, 0, v24
	v_fma_f32 v24, v36, v26, v30
	v_cvt_pk_f16_f32 v85, v54, v55
	v_max_f32_e32 v54, 0, v24
	v_lshlrev_b32_e32 v24, 5, v37
	s_mov_b32 s0, 0x13400
	v_fmac_f32_e32 v31, v36, v27
	v_add3_u32 v28, v24, v38, s0
	ds_read_b128 v[24:27], v94 offset:2048
	s_waitcnt lgkmcnt(1)
	v_mfma_f32_32x32x16_f16 v[0:15], v[48:51], v[44:47], v[0:15]
	v_max_f32_e32 v55, 0, v31
	ds_read_b128 v[20:23], v39 offset:1488
	s_barrier
	ds_read_b128 v[88:91], v28
	ds_read_b128 v[28:31], v94 offset:3072
	v_cvt_pk_f16_f32 v37, v54, v55
	v_cmp_gt_u32_e32 vcc, 32, v92
	s_waitcnt lgkmcnt(2)
	v_fma_f32 v20, v36, v32, v20
	v_mfma_f32_32x32x16_f16 v[0:15], v[24:27], v[84:87], v[0:15]
	v_fma_f32 v21, v36, v33, v21
	v_fma_f32 v22, v36, v34, v22
	v_fmac_f32_e32 v23, v36, v35
	v_max_f32_e32 v20, 0, v20
	v_max_f32_e32 v21, 0, v21
	v_max_f32_e32 v22, 0, v22
	v_max_f32_e32 v23, 0, v23
	v_cvt_pk_f16_f32 v39, v22, v23
	v_cvt_pk_f16_f32 v38, v20, v21
	v_cvt_pk_f16_f32 v36, v52, v53
	ds_read_b128 v[20:23], v94 offset:4096
	ds_read_b128 v[32:35], v94 offset:5120
	s_waitcnt lgkmcnt(2)
	v_mfma_f32_32x32x16_f16 v[0:15], v[28:31], v[36:39], v[0:15]
	s_waitcnt lgkmcnt(1)
	v_mfma_f32_32x32x16_f16 v[0:15], v[20:23], v[88:91], v[0:15]
	ds_read_b128 v[20:23], v93 offset:160
	ds_read_b128 v[24:27], v93 offset:192
	ds_read_b128 v[28:31], v93 offset:224
	ds_read_b128 v[64:67], v93 offset:256
	s_waitcnt lgkmcnt(1)
	v_mfma_f32_32x32x16_f16 v[16:31], v[32:35], v[40:43], v[16:31]
	ds_read_b128 v[32:35], v94 offset:6144
	ds_read_b128 v[48:51], v94 offset:7168
	s_nop 3
	s_nop 0
	s_nop 0
	s_nop 0
	s_nop 0
	v_max_f32_e32 v4, 0, v4
	v_max_f32_e32 v5, 0, v5
	s_waitcnt lgkmcnt(1)
	v_mfma_f32_32x32x16_f16 v[16:31], v[32:35], v[44:47], v[16:31]
	v_max_f32_e32 v6, 0, v6
	v_max_f32_e32 v7, 0, v7
	s_nop 0
	s_nop 0
	v_max_f32_e32 v2, 0, v2
	v_max_f32_e32 v3, 0, v3
	s_nop 0
	s_waitcnt lgkmcnt(0)
	v_mfma_f32_32x32x16_f16 v[16:31], v[48:51], v[84:87], v[16:31]
	ds_read_b128 v[32:35], v94 offset:8192
	ds_read_b128 v[48:51], v94 offset:9216
	s_nop 0
	v_max_f32_e32 v0, 0, v0
	v_max_f32_e32 v1, 0, v1
	s_waitcnt lgkmcnt(1)
	v_mfma_f32_32x32x16_f16 v[16:31], v[32:35], v[36:39], v[16:31]
	ds_read_b128 v[32:35], v94 offset:10240
	s_waitcnt lgkmcnt(1)
	v_mfma_f32_32x32x16_f16 v[16:31], v[48:51], v[88:91], v[16:31]
	ds_read_b128 v[68:71], v93 offset:288
	ds_read_b128 v[72:75], v93 offset:320
	ds_read_b128 v[76:79], v93 offset:352
	ds_read_b128 v[48:51], v93 offset:384
	ds_read_b128 v[52:55], v94 offset:11264
	s_waitcnt lgkmcnt(2)
	v_mfma_f32_32x32x16_f16 v[64:79], v[32:35], v[40:43], v[64:79]
	s_waitcnt lgkmcnt(0)
	v_mfma_f32_32x32x16_f16 v[64:79], v[52:55], v[44:47], v[64:79]
	ds_read_b128 v[32:35], v94 offset:12288
	ds_read_b128 v[52:55], v94 offset:13312
	s_waitcnt lgkmcnt(1)
	v_mfma_f32_32x32x16_f16 v[64:79], v[32:35], v[84:87], v[64:79]
	ds_read_b128 v[32:35], v94 offset:14336
	ds_read_b128 v[96:99], v94 offset:15360
	s_waitcnt lgkmcnt(2)
	v_mfma_f32_32x32x16_f16 v[64:79], v[52:55], v[36:39], v[64:79]
	s_waitcnt lgkmcnt(1)
	v_mfma_f32_32x32x16_f16 v[64:79], v[32:35], v[88:91], v[64:79]
	ds_read_b128 v[52:55], v93 offset:416
	ds_read_b128 v[56:59], v93 offset:448
	ds_read_b128 v[60:63], v93 offset:480
	ds_read_b128 v[32:35], v93 offset:512
	s_waitcnt lgkmcnt(1)
	v_mfma_f32_32x32x16_f16 v[48:63], v[96:99], v[40:43], v[48:63]
	ds_read_b128 v[40:43], v94 offset:16384
	ds_read_b128 v[96:99], v94 offset:17408
	s_waitcnt lgkmcnt(1)
	v_mfma_f32_32x32x16_f16 v[48:63], v[40:43], v[44:47], v[48:63]
	ds_read_b128 v[40:43], v94 offset:18432
	ds_read_b128 v[44:47], v94 offset:19456
	s_waitcnt lgkmcnt(2)
	v_mfma_f32_32x32x16_f16 v[48:63], v[96:99], v[84:87], v[48:63]
	v_cvt_pk_f16_f32 v87, v6, v7
	v_cvt_pk_f16_f32 v86, v4, v5
	s_nop 0
	s_nop 0
	s_nop 0
	s_nop 0
	v_max_f32_e32 v4, 0, v12
	s_waitcnt lgkmcnt(1)
	v_mfma_f32_32x32x16_f16 v[48:63], v[40:43], v[36:39], v[48:63]
	v_max_f32_e32 v5, 0, v13
	v_max_f32_e32 v6, 0, v14
	v_max_f32_e32 v7, 0, v15
	v_cvt_pk_f16_f32 v85, v2, v3
	s_nop 0
	s_nop 0
	v_max_f32_e32 v2, 0, v10
	s_waitcnt lgkmcnt(0)
	v_mfma_f32_32x32x16_f16 v[48:63], v[44:47], v[88:91], v[48:63]
	v_cvt_pk_f16_f32 v91, v6, v7
	v_cvt_pk_f16_f32 v90, v4, v5
	s_nop 0
	s_nop 0
	s_nop 0
	s_nop 0
	v_max_f32_e32 v3, 0, v11
	v_max_f32_e32 v4, 0, v20
	v_max_f32_e32 v5, 0, v21
	v_max_f32_e32 v6, 0, v22
	v_max_f32_e32 v7, 0, v23
	v_cvt_pk_f16_f32 v89, v2, v3
	v_max_f32_e32 v2, v18, v18
	v_max_f32_e32 v3, v19, v19
	v_cvt_pk_f16_f32 v19, v6, v7
	v_cvt_pk_f16_f32 v18, v4, v5
	s_nop 0
	s_nop 0
	s_nop 0
	s_nop 0
	v_max_f32_e32 v4, 0, v28
	v_max_f32_e32 v5, 0, v29
	v_max_f32_e32 v6, 0, v30
	v_max_f32_e32 v7, 0, v31
	v_cvt_pk_f16_f32 v84, v0, v1
	s_nop 0
	s_nop 0
	v_cvt_pk_f16_f32 v23, v6, v7
	v_cvt_pk_f16_f32 v22, v4, v5
	s_nop 0
	s_nop 0
	s_nop 0
	s_nop 0
	v_max_f32_e32 v0, 0, v8
	v_max_f32_e32 v1, 0, v9
	v_max_f32_e32 v2, 0, v2
	v_max_f32_e32 v3, 0, v3
	v_max_f32_e32 v4, 0, v68
	v_max_f32_e32 v5, 0, v69
	v_max_f32_e32 v6, 0, v70
	v_max_f32_e32 v7, 0, v71
	v_cvt_pk_f16_f32 v88, v0, v1
	s_nop 0
	v_max_f32_e32 v1, v17, v17
	v_cvt_pk_f16_f32 v17, v2, v3
	v_max_f32_e32 v2, v26, v26
	v_max_f32_e32 v3, v27, v27
	v_cvt_pk_f16_f32 v27, v6, v7
	v_cvt_pk_f16_f32 v26, v4, v5
	ds_read_b128 v[4:7], v94 offset:20480
	v_max_f32_e32 v0, 0, v16
	v_max_f32_e32 v1, 0, v1
	v_cvt_pk_f16_f32 v16, v0, v1
	s_nop 0
	s_nop 0
	v_max_f32_e32 v0, 0, v24
	v_max_f32_e32 v1, 0, v25
	v_cvt_pk_f16_f32 v20, v0, v1
	s_nop 0
	s_nop 0
	ds_read_b128 v[36:39], v93 offset:544
	ds_read_b128 v[40:43], v93 offset:576
	ds_read_b128 v[44:47], v93 offset:608
	v_max_f32_e32 v0, 0, v64
	v_max_f32_e32 v1, 0, v65
	v_cvt_pk_f16_f32 v24, v0, v1
	s_nop 0
	v_max_f32_e32 v2, 0, v2
	v_max_f32_e32 v3, 0, v3
	v_max_f32_e32 v12, 0, v72
	s_nop 0
	v_cvt_pk_f16_f32 v21, v2, v3
	s_nop 0
	s_nop 0
	v_max_f32_e32 v13, 0, v73
	s_nop 0
	v_max_f32_e32 v2, 0, v66
	v_max_f32_e32 v3, 0, v67
	v_max_f32_e32 v14, 0, v74
	s_nop 0
	s_waitcnt lgkmcnt(0)
	v_mfma_f32_32x32x16_f16 v[32:47], v[4:7], v[84:87], v[32:47]
	v_cvt_pk_f16_f32 v25, v2, v3
	v_max_f32_e32 v15, 0, v75
	s_nop 0
	s_nop 0
	s_nop 0
	s_nop 0
	v_max_f32_e32 v0, 0, v76
	v_max_f32_e32 v1, 0, v77
	v_max_f32_e32 v2, 0, v78
	v_max_f32_e32 v3, 0, v79
	v_cvt_pk_f16_f32 v31, v2, v3
	v_cvt_pk_f16_f32 v30, v0, v1
	ds_read_b128 v[0:3], v93 offset:640
	ds_read_b128 v[8:11], v94 offset:21504
	s_nop 0
	v_cvt_pk_f16_f32 v28, v12, v13
	v_max_f32_e32 v12, 0, v48
	s_nop 0
	v_max_f32_e32 v13, 0, v49
	ds_read_b128 v[4:7], v94 offset:22528
	s_waitcnt lgkmcnt(1)
	v_mfma_f32_32x32x16_f16 v[32:47], v[8:11], v[88:91], v[32:47]
	s_nop 0
	v_cvt_pk_f16_f32 v29, v14, v15
	v_max_f32_e32 v14, 0, v50
	s_nop 0
	v_max_f32_e32 v15, 0, v51
	s_nop 0
	v_max_f32_e32 v48, 0, v52
	ds_read_b128 v[8:11], v94 offset:23552
	s_waitcnt lgkmcnt(1)
	v_mfma_f32_32x32x16_f16 v[32:47], v[4:7], v[16:19], v[32:47]
	s_nop 0
	v_max_f32_e32 v49, 0, v53
	s_nop 0
	v_max_f32_e32 v50, 0, v54
	s_nop 0
	v_max_f32_e32 v51, 0, v55
	ds_read_b128 v[4:7], v94 offset:24576
	s_waitcnt lgkmcnt(1)
	v_mfma_f32_32x32x16_f16 v[32:47], v[8:11], v[20:23], v[32:47]
	s_nop 0
	v_cvt_pk_f16_f32 v51, v50, v51
	v_cvt_pk_f16_f32 v50, v48, v49
	v_cvt_pk_f16_f32 v48, v12, v13
	v_max_f32_e32 v12, 0, v56
	ds_read_b128 v[8:11], v94 offset:25600
	v_cvt_pk_f16_f32 v49, v14, v15
	s_waitcnt lgkmcnt(1)
	v_mfma_f32_32x32x16_f16 v[32:47], v[4:7], v[24:27], v[32:47]
	s_nop 0
	v_max_f32_e32 v13, 0, v57
	s_nop 0
	v_max_f32_e32 v14, 0, v58
	s_nop 0
	v_max_f32_e32 v15, 0, v59
	ds_read_b128 v[4:7], v94 offset:26624
	s_waitcnt lgkmcnt(1)
	v_mfma_f32_32x32x16_f16 v[32:47], v[8:11], v[28:31], v[32:47]
	s_nop 0
	v_max_f32_e32 v52, 0, v60
	s_nop 0
	v_max_f32_e32 v53, 0, v61
	s_nop 0
	v_max_f32_e32 v54, 0, v62
	ds_read_b128 v[8:11], v94 offset:27648
	s_waitcnt lgkmcnt(1)
	v_mfma_f32_32x32x16_f16 v[32:47], v[4:7], v[48:51], v[32:47]
	ds_read_b128 v[56:59], v94 offset:28672
	s_nop 0
	v_max_f32_e32 v4, 0, v63
	v_cvt_pk_f16_f32 v55, v54, v4
	v_cvt_pk_f16_f32 v54, v52, v53
	v_cvt_pk_f16_f32 v53, v14, v15
	v_cvt_pk_f16_f32 v52, v12, v13
	s_waitcnt lgkmcnt(1)
	s_nop 0
	v_mfma_f32_32x32x16_f16 v[32:47], v[8:11], v[52:55], v[32:47]
	ds_read_b128 v[4:7], v93 offset:672
	ds_read_b128 v[8:11], v93 offset:704
	ds_read_b128 v[12:15], v93 offset:736
	ds_read_b128 v[60:63], v94 offset:29696
	ds_read_b128 v[64:67], v93 offset:768
	s_waitcnt lgkmcnt(2)
	v_mfma_f32_32x32x16_f16 v[0:15], v[56:59], v[84:87], v[0:15]
	s_waitcnt lgkmcnt(1)
	v_mfma_f32_32x32x16_f16 v[0:15], v[60:63], v[88:91], v[0:15]
	ds_read_b128 v[56:59], v94 offset:30720
	ds_read_b128 v[60:63], v94 offset:31744
	s_waitcnt lgkmcnt(1)
	v_mfma_f32_32x32x16_f16 v[0:15], v[56:59], v[16:19], v[0:15]
	s_waitcnt lgkmcnt(0)
	v_mfma_f32_32x32x16_f16 v[0:15], v[60:63], v[20:23], v[0:15]
	ds_read_b128 v[16:19], v94 offset:32768
	ds_read_b128 v[20:23], v94 offset:33792
	s_waitcnt lgkmcnt(1)
	v_mfma_f32_32x32x16_f16 v[0:15], v[16:19], v[24:27], v[0:15]
	s_waitcnt lgkmcnt(0)
	v_mfma_f32_32x32x16_f16 v[0:15], v[20:23], v[28:31], v[0:15]
	ds_read_b128 v[16:19], v94 offset:34816
	ds_read_b128 v[20:23], v94 offset:35840
	s_waitcnt lgkmcnt(1)
	v_mfma_f32_32x32x16_f16 v[0:15], v[16:19], v[48:51], v[0:15]
	s_nop 0
	v_max_f32_e32 v16, 0, v32
	s_nop 0
	v_fma_f32 v16, v64, v16, 0
	v_max_f32_e32 v17, 0, v33
	v_fmac_f32_e32 v16, v65, v17
	s_nop 0
	s_waitcnt lgkmcnt(0)
	v_mfma_f32_32x32x16_f16 v[0:15], v[20:23], v[52:55], v[0:15]
	v_max_f32_e32 v17, 0, v34
	ds_read_b128 v[18:21], v93 offset:800
	ds_read_b128 v[22:25], v93 offset:832
	v_fmac_f32_e32 v16, v66, v17
	s_nop 0
	v_max_f32_e32 v17, 0, v35
	v_fmac_f32_e32 v16, v67, v17
	s_nop 0
	v_max_f32_e32 v17, 0, v36
	s_waitcnt lgkmcnt(1)
	v_fmac_f32_e32 v16, v18, v17
	s_nop 0
	v_max_f32_e32 v17, 0, v37
	v_fmac_f32_e32 v16, v19, v17
	s_nop 0
	v_max_f32_e32 v17, 0, v38
	v_fmac_f32_e32 v16, v20, v17
	s_nop 0
	v_max_f32_e32 v17, 0, v39
	v_fmac_f32_e32 v16, v21, v17
	s_nop 0
	v_max_f32_e32 v17, 0, v40
	s_waitcnt lgkmcnt(0)
	v_fmac_f32_e32 v16, v22, v17
	s_nop 0
	v_max_f32_e32 v17, 0, v41
	v_fmac_f32_e32 v16, v23, v17
	s_nop 0
	v_max_f32_e32 v17, 0, v42
	ds_read_b128 v[18:21], v93 offset:864
	v_fmac_f32_e32 v16, v24, v17
	s_nop 0
	v_max_f32_e32 v17, 0, v43
	v_fmac_f32_e32 v16, v25, v17
	s_nop 0
	v_max_f32_e32 v17, 0, v44
	ds_read_b128 v[22:25], v93 offset:896
	s_waitcnt lgkmcnt(1)
	v_fmac_f32_e32 v16, v18, v17
	s_nop 0
	v_max_f32_e32 v17, 0, v45
	v_fmac_f32_e32 v16, v19, v17
	s_nop 0
	v_max_f32_e32 v17, 0, v46
	v_fmac_f32_e32 v16, v20, v17
	s_nop 0
	v_max_f32_e32 v17, 0, v47
	s_nop 0
	v_fmac_f32_e32 v16, v21, v17
	v_max_f32_e32 v0, 0, v0
	s_waitcnt lgkmcnt(0)
	v_fmac_f32_e32 v16, v22, v0
	s_nop 0
	v_max_f32_e32 v0, 0, v1
	v_fmac_f32_e32 v16, v23, v0
	s_nop 0
	v_max_f32_e32 v0, 0, v2
	v_fmac_f32_e32 v16, v24, v0
	s_nop 0
	v_max_f32_e32 v17, 0, v3
	ds_read_b128 v[0:3], v93 offset:928
	ds_read_b128 v[18:21], v93 offset:960
	s_nop 0
	v_fmac_f32_e32 v16, v25, v17
	v_max_f32_e32 v4, 0, v4
	s_waitcnt lgkmcnt(1)
	v_fmac_f32_e32 v16, v0, v4
	s_nop 0
	v_max_f32_e32 v0, 0, v5
	v_fmac_f32_e32 v16, v1, v0
	s_nop 0
	v_max_f32_e32 v0, 0, v6
	v_fmac_f32_e32 v16, v2, v0
	s_nop 0
	v_max_f32_e32 v0, 0, v7
	v_fmac_f32_e32 v16, v3, v0
	s_nop 0
	v_max_f32_e32 v0, 0, v8
	s_waitcnt lgkmcnt(0)
	v_fmac_f32_e32 v16, v18, v0
	s_nop 0
	v_max_f32_e32 v0, 0, v9
	v_fmac_f32_e32 v16, v19, v0
	s_nop 0
	v_max_f32_e32 v0, 0, v10
	v_fmac_f32_e32 v16, v20, v0
	s_nop 0
	v_max_f32_e32 v0, 0, v11
	v_fmac_f32_e32 v16, v21, v0
	s_nop 0
	v_max_f32_e32 v0, 0, v12
	v_fmac_f32_e32 v16, v80, v0
	s_nop 0
	v_max_f32_e32 v0, 0, v13
	v_fmac_f32_e32 v16, v81, v0
	s_nop 0
	v_max_f32_e32 v0, 0, v14
	v_fmac_f32_e32 v16, v82, v0
	s_nop 0
	v_max_f32_e32 v0, 0, v15
	v_fmac_f32_e32 v16, v83, v0
	v_mov_b32_e32 v0, v16
	s_nop 1
	v_permlane32_swap_b32_e32 v16, v0
	s_and_saveexec_b64 s[0:1], vcc
	s_cbranch_execz .LBB0_123
	s_mov_b32 s0, s88
	v_add_f32_e32 v0, v16, v0
	s_waitcnt lgkmcnt(0)
	v_add_f32_e32 v0, s0, v0
	v_mul_f32_e32 v0, 0xbfb8aa3b, v0
	v_exp_f32_e32 v1, v0
	s_or_b32 s0, s31, s30
	v_or_b32_e32 v0, s0, v92
	v_add_f32_e32 v2, 1.0, v1
	v_div_scale_f32 v3, s[0:1], v2, v2, 1.0
	v_rcp_f32_e32 v4, v3
	v_div_scale_f32 v5, vcc, 1.0, v2, 1.0
	v_ashrrev_i32_e32 v1, 31, v0
	v_fma_f32 v6, -v3, v4, 1.0
	v_fmac_f32_e32 v4, v6, v4
	v_mul_f32_e32 v6, v5, v4
	v_fma_f32 v7, -v3, v6, v5
	v_fmac_f32_e32 v6, v7, v4
	v_fma_f32 v3, -v3, v6, v5
	v_div_fmas_f32 v3, v3, v4, v6
	v_div_fixup_f32 v2, v3, v2, 1.0
	v_lshl_add_u64 v[0:1], v[0:1], 2, s[22:23]
	global_store_dword v[0:1], v2, off
